# v13: v10 + expert gate/up epilogue biases prefetched at unit start (no drain at the epilogue head), mLSTM state-scan loads all in flight, ph6 n-state load hoisted next to the other unit loads
# baseline (speedup 1.0000x reference)
; __device__ __forceinline__ void ph5_m2(const Frame& F, const Args& A) {
;     ...
;     for (int task0 = F.vcu; task0 < NT_C; task0 += 2 * F.G) {
;         const bool hasB = task0 + F.G < NT_C;
;         const int ttA = task0, ttB = hasB ? task0 + F.G : task0;
;         const int hA = ttA >> 6, rA = (ttA * 128 + 2 * l) & 8191, jA = ttA & 63, hB = ttB >> 6, rB = (ttB * 128 + 2 * l) & 8191, jB = ttB & 63;
;         const bf16* srcA = U + (size_t)hA * 128 * 8192 + rA; const bf16* srcB = U + (size_t)hB * 128 * 8192 + rB;
;         const float* snA = UN + (size_t)hA * 128 * 64 + jA; const float* snB = UN + (size_t)hB * 128 * 64 + jB;
;         f32x2_t uA[16], uB[16]; float nA[16], nB[16];
; #pragma unroll
;         for (int i = 0; i < 16; ++i) { const unsigned wa = *(const unsigned*)(srcA + (size_t)(16 * g + i) * 8192), wb = *(const unsigned*)(srcB + (size_t)(16 * g + i) * 8192);
;             uA[i] = (f32x2_t){bflo(wa), bfhi(wa)}; uB[i] = (f32x2_t){bflo(wb), bfhi(wb)};
;             nA[i] = snA[(16 * g + i) * 64]; nB[i] = snB[(16 * g + i) * 64]; }
.LBB0_583:
	v_readlane_b32 s4, v254, 49
	s_add_i32 s6, s89, s4
	s_cmpk_lt_i32 s6, 0x200
	s_cselect_b64 s[50:51], -1, 0
	s_and_b64 s[4:5], s[50:51], exec
	s_cselect_b32 s5, s6, s89
	s_ashr_i32 s4, s89, 6
	s_lshl_b32 s6, s89, 7
	s_lshl_b32 s8, s5, 7
	s_and_b32 s6, s6, 0x1f80
	s_ashr_i32 s92, s5, 6
	s_and_b32 s8, s8, 0x1f80
	s_and_b32 s11, s5, 63
	s_ashr_i32 s5, s4, 31
	v_or_b32_e32 v2, s6, v75
	s_and_b32 s6, s89, 63
	v_or_b32_e32 v4, s8, v75
	s_lshl_b64 s[8:9], s[4:5], 21
	v_readlane_b32 s10, v255, 7
	s_add_u32 s8, s10, s8
	v_readlane_b32 s12, v255, 9
	s_addc_u32 s9, s12, s9
	v_lshlrev_b32_e32 v2, 1, v2
	s_ashr_i32 s93, s92, 31
	v_lshl_add_u64 v[66:67], s[8:9], 0, v[2:3]
	s_lshl_b64 s[8:9], s[92:93], 21
	s_add_u32 s8, s10, s8
	s_addc_u32 s9, s12, s9
	v_lshlrev_b32_e32 v62, 1, v4
	v_mov_b32_e32 v63, v3
	v_lshl_add_u64 v[68:69], s[8:9], 0, v[62:63]
	s_lshl_b64 s[8:9], s[4:5], 15
	v_readlane_b32 s14, v255, 11
	s_add_u32 s8, s14, s8
	v_readlane_b32 s15, v255, 13
	s_addc_u32 s10, s15, s9
	s_lshl_b32 s44, s6, 2
	s_add_u32 s9, s8, s44
	s_addc_u32 s10, s10, 0
	s_lshl_b64 s[12:13], s[92:93], 15
	s_add_u32 s6, s14, s12
	s_addc_u32 s8, s15, s13
	s_lshl_b32 s56, s11, 2
	v_readlane_b32 s12, v254, 52
	s_add_u32 s6, s6, s56
	v_readlane_b32 s13, v254, 53
	s_addc_u32 s8, s8, 0
	s_lshl_b64 s[12:13], s[12:13], 1
	s_mov_b32 s98, 0x4000
	s_mov_b32 s99, 0
	v_lshl_add_u64 v[166:167], v[66:67], 0, s[12:13]
	v_lshl_add_u64 v[168:169], v[68:69], 0, s[12:13]
	global_load_dword v134, v[166:167], off
	global_load_dword v135, v[168:169], off
	v_lshl_add_u64 v[166:167], v[166:167], 0, s[98:99]
	v_lshl_add_u64 v[168:169], v[168:169], 0, s[98:99]
	global_load_dword v136, v[166:167], off
	global_load_dword v137, v[168:169], off
	v_lshl_add_u64 v[166:167], v[166:167], 0, s[98:99]
	v_lshl_add_u64 v[168:169], v[168:169], 0, s[98:99]
	global_load_dword v138, v[166:167], off
	global_load_dword v139, v[168:169], off
	v_lshl_add_u64 v[166:167], v[166:167], 0, s[98:99]
	v_lshl_add_u64 v[168:169], v[168:169], 0, s[98:99]
	global_load_dword v140, v[166:167], off
	global_load_dword v141, v[168:169], off
	v_lshl_add_u64 v[166:167], v[166:167], 0, s[98:99]
	v_lshl_add_u64 v[168:169], v[168:169], 0, s[98:99]
	global_load_dword v142, v[166:167], off
	global_load_dword v143, v[168:169], off
	v_lshl_add_u64 v[166:167], v[166:167], 0, s[98:99]
	v_lshl_add_u64 v[168:169], v[168:169], 0, s[98:99]
	global_load_dword v144, v[166:167], off
	global_load_dword v145, v[168:169], off
	v_lshl_add_u64 v[166:167], v[166:167], 0, s[98:99]
	v_lshl_add_u64 v[168:169], v[168:169], 0, s[98:99]
	global_load_dword v146, v[166:167], off
	global_load_dword v147, v[168:169], off
	v_lshl_add_u64 v[166:167], v[166:167], 0, s[98:99]
	v_lshl_add_u64 v[168:169], v[168:169], 0, s[98:99]
	global_load_dword v148, v[166:167], off
	global_load_dword v149, v[168:169], off
	v_lshl_add_u64 v[166:167], v[166:167], 0, s[98:99]
	v_lshl_add_u64 v[168:169], v[168:169], 0, s[98:99]
	global_load_dword v150, v[166:167], off
	global_load_dword v151, v[168:169], off
	v_lshl_add_u64 v[166:167], v[166:167], 0, s[98:99]
	v_lshl_add_u64 v[168:169], v[168:169], 0, s[98:99]
	global_load_dword v152, v[166:167], off
	global_load_dword v153, v[168:169], off
	v_lshl_add_u64 v[166:167], v[166:167], 0, s[98:99]
	v_lshl_add_u64 v[168:169], v[168:169], 0, s[98:99]
	global_load_dword v154, v[166:167], off
	global_load_dword v155, v[168:169], off
	v_lshl_add_u64 v[166:167], v[166:167], 0, s[98:99]
	v_lshl_add_u64 v[168:169], v[168:169], 0, s[98:99]
	global_load_dword v156, v[166:167], off
	global_load_dword v157, v[168:169], off
	v_lshl_add_u64 v[166:167], v[166:167], 0, s[98:99]
	v_lshl_add_u64 v[168:169], v[168:169], 0, s[98:99]
	global_load_dword v158, v[166:167], off
	global_load_dword v159, v[168:169], off
	v_lshl_add_u64 v[166:167], v[166:167], 0, s[98:99]
	v_lshl_add_u64 v[168:169], v[168:169], 0, s[98:99]
	global_load_dword v160, v[166:167], off
	global_load_dword v161, v[168:169], off
	v_lshl_add_u64 v[166:167], v[166:167], 0, s[98:99]
	v_lshl_add_u64 v[168:169], v[168:169], 0, s[98:99]
	global_load_dword v162, v[166:167], off
	global_load_dword v163, v[168:169], off
	v_lshl_add_u64 v[166:167], v[166:167], 0, s[98:99]
	v_lshl_add_u64 v[168:169], v[168:169], 0, s[98:99]
	global_load_dword v164, v[166:167], off
	global_load_dword v165, v[168:169], off
	s_waitcnt vmcnt(0)
; __device__ __forceinline__ void ph5_m2(const Frame& F, const Args& A) {
;     ...
; #pragma unroll
;         for (int i = 0; i < 16; ++i) { const unsigned wa = *(const unsigned*)(srcA + (size_t)(16 * g + i) * 8192), wb = *(const unsigned*)(srcB + (size_t)(16 * g + i) * 8192);
;             uA[i] = (f32x2_t){bflo(wa), bfhi(wa)}; uB[i] = (f32x2_t){bflo(wb), bfhi(wb)};
;             nA[i] = snA[(16 * g + i) * 64]; nB[i] = snB[(16 * g + i) * 64]; }
	v_lshl_add_u64 v[4:5], v[66:67], 0, s[12:13]
	v_mov_b32_e32 v6, v134
	v_lshl_add_u64 v[4:5], v[68:69], 0, s[12:13]
	v_mov_b32_e32 v4, v135
	s_add_u32 s12, s9, s48
	s_addc_u32 s13, s10, s49
	global_load_dword v82, v3, s[12:13]
	s_add_u32 s12, s6, s48
	s_addc_u32 s13, s8, s49
	global_load_dword v113, v3, s[12:13]
	v_readlane_b32 s12, v254, 54
	v_readlane_b32 s13, v254, 55
	s_lshl_b64 s[12:13], s[12:13], 1
	s_mov_b64 s[24:25], s[18:19]
	s_mov_b64 s[22:23], s[20:21]
	v_readlane_b32 s16, v255, 15
	v_readlane_b32 s17, v255, 16
	v_lshlrev_b32_e32 v64, 16, v6
	v_and_b32_e32 v65, 0xffff0000, v6
	v_lshlrev_b32_e32 v58, 16, v4
	v_and_b32_e32 v59, 0xffff0000, v4
	v_lshl_add_u64 v[4:5], v[66:67], 0, s[12:13]
	v_mov_b32_e32 v6, v136
	v_lshl_add_u64 v[4:5], v[68:69], 0, s[12:13]
	v_mov_b32_e32 v4, v137
	s_add_u32 s12, s9, s52
	s_addc_u32 s13, s10, s53
	global_load_dword v114, v3, s[12:13]
	s_add_u32 s12, s6, s52
	s_addc_u32 s13, s8, s53
	global_load_dword v111, v3, s[12:13]
	v_readlane_b32 s12, v254, 56
	v_readlane_b32 s13, v254, 57
	s_lshl_b64 s[12:13], s[12:13], 1
	v_lshlrev_b32_e32 v60, 16, v6
	v_and_b32_e32 v61, 0xffff0000, v6
	v_lshlrev_b32_e32 v54, 16, v4
	v_and_b32_e32 v55, 0xffff0000, v4
	v_lshl_add_u64 v[4:5], v[66:67], 0, s[12:13]
	v_mov_b32_e32 v6, v138
	v_lshl_add_u64 v[4:5], v[68:69], 0, s[12:13]
	v_mov_b32_e32 v4, v139
	s_add_u32 s12, s9, s54
	s_addc_u32 s13, s10, s55
	global_load_dword v112, v3, s[12:13]
	s_add_u32 s12, s6, s54
	s_addc_u32 s13, s8, s55
	global_load_dword v109, v3, s[12:13]
	s_lshl_b64 s[12:13], s[20:21], 1
	v_lshlrev_b32_e32 v56, 16, v6
	v_and_b32_e32 v57, 0xffff0000, v6
	v_lshlrev_b32_e32 v50, 16, v4
	v_and_b32_e32 v51, 0xffff0000, v4
	v_lshl_add_u64 v[4:5], v[66:67], 0, s[12:13]
	v_mov_b32_e32 v6, v140
	v_lshl_add_u64 v[4:5], v[68:69], 0, s[12:13]
	v_mov_b32_e32 v4, v141
	s_add_u32 s12, s9, s58
	s_addc_u32 s13, s10, s59
	global_load_dword v110, v3, s[12:13]
	s_add_u32 s12, s6, s58
	s_addc_u32 s13, s8, s59
	global_load_dword v107, v3, s[12:13]
	s_lshl_b64 s[12:13], s[18:19], 1
	v_lshlrev_b32_e32 v52, 16, v6
	v_and_b32_e32 v53, 0xffff0000, v6
	v_lshlrev_b32_e32 v46, 16, v4
	v_and_b32_e32 v47, 0xffff0000, v4
	v_lshl_add_u64 v[4:5], v[66:67], 0, s[12:13]
	v_mov_b32_e32 v6, v142
	v_lshl_add_u64 v[4:5], v[68:69], 0, s[12:13]
	v_mov_b32_e32 v4, v143
	s_add_u32 s12, s9, s60
	s_addc_u32 s13, s10, s61
	global_load_dword v108, v3, s[12:13]
	s_add_u32 s12, s6, s60
	s_addc_u32 s13, s8, s61
	global_load_dword v105, v3, s[12:13]
	v_readlane_b32 s12, v254, 58
	v_readlane_b32 s13, v254, 59
	s_lshl_b64 s[12:13], s[12:13], 1
	v_lshlrev_b32_e32 v48, 16, v6
	v_and_b32_e32 v49, 0xffff0000, v6
	v_lshlrev_b32_e32 v42, 16, v4
	v_and_b32_e32 v43, 0xffff0000, v4
	v_lshl_add_u64 v[4:5], v[66:67], 0, s[12:13]
	v_mov_b32_e32 v6, v144
	v_lshl_add_u64 v[4:5], v[68:69], 0, s[12:13]
	v_mov_b32_e32 v4, v145
	s_add_u32 s12, s9, s62
	s_addc_u32 s13, s10, s63
	global_load_dword v106, v3, s[12:13]
	s_add_u32 s12, s6, s62
	s_addc_u32 s13, s8, s63
	global_load_dword v103, v3, s[12:13]
	v_readlane_b32 s12, v254, 60
	v_readlane_b32 s13, v254, 61
	s_lshl_b64 s[12:13], s[12:13], 1
	v_lshlrev_b32_e32 v44, 16, v6
	v_and_b32_e32 v45, 0xffff0000, v6
	v_lshlrev_b32_e32 v38, 16, v4
	v_and_b32_e32 v39, 0xffff0000, v4
	v_lshl_add_u64 v[4:5], v[66:67], 0, s[12:13]
	v_mov_b32_e32 v6, v146
	v_lshl_add_u64 v[4:5], v[68:69], 0, s[12:13]
	v_mov_b32_e32 v4, v147
	s_add_u32 s12, s9, s64
	s_addc_u32 s13, s10, s65
	global_load_dword v104, v3, s[12:13]
	s_add_u32 s12, s6, s64
	s_addc_u32 s13, s8, s65
	global_load_dword v101, v3, s[12:13]
	v_readlane_b32 s12, v254, 62
	v_readlane_b32 s13, v254, 63
	s_lshl_b64 s[12:13], s[12:13], 1
	v_lshlrev_b32_e32 v40, 16, v6
	v_and_b32_e32 v41, 0xffff0000, v6
	v_lshlrev_b32_e32 v34, 16, v4
	v_and_b32_e32 v35, 0xffff0000, v4
	v_lshl_add_u64 v[4:5], v[66:67], 0, s[12:13]
	v_mov_b32_e32 v6, v148
	v_lshl_add_u64 v[4:5], v[68:69], 0, s[12:13]
	v_mov_b32_e32 v4, v149
	s_add_u32 s12, s9, s66
	s_addc_u32 s13, s10, s67
	global_load_dword v102, v3, s[12:13]
	s_add_u32 s12, s6, s66
	s_addc_u32 s13, s8, s67
	global_load_dword v99, v3, s[12:13]
	s_lshl_b64 s[12:13], s[26:27], 1
	v_lshlrev_b32_e32 v36, 16, v6
	v_and_b32_e32 v37, 0xffff0000, v6
	v_lshlrev_b32_e32 v30, 16, v4
	v_and_b32_e32 v31, 0xffff0000, v4
	v_lshl_add_u64 v[4:5], v[66:67], 0, s[12:13]
	v_mov_b32_e32 v6, v150
	v_lshl_add_u64 v[4:5], v[68:69], 0, s[12:13]
	v_mov_b32_e32 v4, v151
	s_add_u32 s12, s9, s68
	s_addc_u32 s13, s10, s69
	global_load_dword v100, v3, s[12:13]
	s_add_u32 s12, s6, s68
	s_addc_u32 s13, s8, s69
	global_load_dword v97, v3, s[12:13]
	s_lshl_b64 s[12:13], s[28:29], 1
	v_lshlrev_b32_e32 v32, 16, v6
	v_and_b32_e32 v33, 0xffff0000, v6
	v_lshlrev_b32_e32 v26, 16, v4
	v_and_b32_e32 v27, 0xffff0000, v4
	v_lshl_add_u64 v[4:5], v[66:67], 0, s[12:13]
	v_mov_b32_e32 v6, v152
	v_lshl_add_u64 v[4:5], v[68:69], 0, s[12:13]
	v_mov_b32_e32 v4, v153
	s_add_u32 s12, s9, s72
	s_addc_u32 s13, s10, s73
	global_load_dword v98, v3, s[12:13]
	s_add_u32 s12, s6, s72
	s_addc_u32 s13, s8, s73
	global_load_dword v95, v3, s[12:13]
	s_lshl_b64 s[12:13], s[30:31], 1
	v_lshlrev_b32_e32 v28, 16, v6
	v_and_b32_e32 v29, 0xffff0000, v6
	v_lshlrev_b32_e32 v22, 16, v4
	v_and_b32_e32 v23, 0xffff0000, v4
	v_lshl_add_u64 v[4:5], v[66:67], 0, s[12:13]
	v_mov_b32_e32 v6, v154
	v_lshl_add_u64 v[4:5], v[68:69], 0, s[12:13]
	v_mov_b32_e32 v4, v155
	s_add_u32 s12, s9, s76
	s_addc_u32 s13, s10, s77
	global_load_dword v96, v3, s[12:13]
	s_add_u32 s12, s6, s76
	s_addc_u32 s13, s8, s77
	global_load_dword v93, v3, s[12:13]
	s_lshl_b64 s[12:13], s[34:35], 1
	v_lshlrev_b32_e32 v24, 16, v6
	v_and_b32_e32 v25, 0xffff0000, v6
; __device__ __forceinline__ void ph5_m2(const Frame& F, const Args& A) {
;     ...
; #pragma unroll
;         for (int i = 0; i < 16; ++i) { const unsigned wa = *(const unsigned*)(srcA + (size_t)(16 * g + i) * 8192), wb = *(const unsigned*)(srcB + (size_t)(16 * g + i) * 8192);
;             uA[i] = (f32x2_t){bflo(wa), bfhi(wa)}; uB[i] = (f32x2_t){bflo(wb), bfhi(wb)};
;             nA[i] = snA[(16 * g + i) * 64]; nB[i] = snB[(16 * g + i) * 64]; }
;         float ApA = 1.f, ApB = 1.f, BnA = 0.f, BnB = 0.f; f32x2_t BpA = {0.f, 0.f}, BpB = {0.f, 0.f};
; #pragma unroll
;         for (int i = 0; i < 16; ++i) { const float dA = decL[hA * 128 + 16 * g + i], sA = sclL[hA * 128 + 16 * g + i], dB = decL[hB * 128 + 16 * g + i], sB = sclL[hB * 128 + 16 * g + i];
;             ApA *= dA; BpA = BpA * dA + uA[i] * sA; BnA = BnA * dA + nA[i] * sA; ApB *= dB; BpB = BpB * dB + uB[i] * sB; BnB = BnB * dB + nB[i] * sB; }
;         seg[g * 128 + 2 * l] = ApA; seg[1024 + g * 128 + 2 * l] = BpA.x; seg[1024 + g * 128 + 2 * l + 1] = BpA.y; seg[2048 + g * 64 + l] = BnA;
;         seg[3072 + g * 128 + 2 * l] = ApB; seg[3072 + 1024 + g * 128 + 2 * l] = BpB.x; seg[3072 + 1024 + g * 128 + 2 * l + 1] = BpB.y; seg[3072 + 2048 + g * 64 + l] = BnB;
	v_lshlrev_b32_e32 v18, 16, v4
	v_and_b32_e32 v19, 0xffff0000, v4
	v_lshl_add_u64 v[4:5], v[66:67], 0, s[12:13]
	v_mov_b32_e32 v6, v156
	v_lshl_add_u64 v[4:5], v[68:69], 0, s[12:13]
	v_mov_b32_e32 v4, v157
	s_add_u32 s12, s9, s80
	s_addc_u32 s13, s10, s81
	global_load_dword v94, v3, s[12:13]
	s_add_u32 s12, s6, s80
	s_addc_u32 s13, s8, s81
	global_load_dword v91, v3, s[12:13]
	s_lshl_b64 s[12:13], s[36:37], 1
	v_lshlrev_b32_e32 v20, 16, v6
	v_and_b32_e32 v21, 0xffff0000, v6
	v_lshlrev_b32_e32 v14, 16, v4
	v_and_b32_e32 v15, 0xffff0000, v4
	v_lshl_add_u64 v[4:5], v[66:67], 0, s[12:13]
	v_mov_b32_e32 v6, v158
	v_lshl_add_u64 v[4:5], v[68:69], 0, s[12:13]
	v_mov_b32_e32 v4, v159
	s_add_u32 s12, s9, s96
	s_addc_u32 s13, s10, s97
	global_load_dword v92, v3, s[12:13]
	s_add_u32 s12, s6, s96
	s_addc_u32 s13, s8, s97
	global_load_dword v89, v3, s[12:13]
	s_lshl_b64 s[12:13], s[38:39], 1
	v_lshlrev_b32_e32 v16, 16, v6
	v_and_b32_e32 v17, 0xffff0000, v6
	v_lshlrev_b32_e32 v10, 16, v4
	v_and_b32_e32 v11, 0xffff0000, v4
	v_lshl_add_u64 v[4:5], v[66:67], 0, s[12:13]
	v_mov_b32_e32 v6, v160
	v_lshl_add_u64 v[4:5], v[68:69], 0, s[12:13]
	v_mov_b32_e32 v4, v161
	s_add_u32 s12, s9, s84
	s_addc_u32 s13, s10, s85
	global_load_dword v90, v3, s[12:13]
	s_add_u32 s12, s6, s84
	s_addc_u32 s13, s8, s85
	global_load_dword v88, v3, s[12:13]
	s_lshl_b64 s[12:13], s[40:41], 1
	v_lshlrev_b32_e32 v12, 16, v6
	v_and_b32_e32 v13, 0xffff0000, v6
	v_lshlrev_b32_e32 v6, 16, v4
	v_and_b32_e32 v7, 0xffff0000, v4
	v_lshl_add_u64 v[4:5], v[66:67], 0, s[12:13]
	v_mov_b32_e32 v9, v162
	v_lshl_add_u64 v[4:5], v[68:69], 0, s[12:13]
	s_add_u32 s12, s9, s86
	s_addc_u32 s13, s10, s87
	v_mov_b32_e32 v5, v163
	v_lshlrev_b32_e32 v8, 16, v9
	global_load_dword v87, v3, s[12:13]
	s_add_u32 s12, s6, s86
	s_addc_u32 s13, s8, s87
	global_load_dword v86, v3, s[12:13]
	s_lshl_b64 s[12:13], s[42:43], 1
	v_lshl_add_u64 v[66:67], v[66:67], 0, s[12:13]
	v_mov_b32_e32 v63, v164
	v_lshl_add_u64 v[66:67], v[68:69], 0, s[12:13]
	s_add_u32 s12, s9, s94
	s_addc_u32 s13, s10, s95
	v_mov_b32_e32 v67, v165
	s_add_u32 s10, s6, s94
	s_addc_u32 s11, s8, s95
	global_load_dword v78, v3, s[10:11]
	s_lshl_b32 s6, s4, 7
	s_add_i32 s6, s6, s0
	s_lshl_b32 s8, s92, 7
	s_lshl_b32 s57, s6, 2
	s_add_i32 s8, s8, s0
	s_add_i32 s18, s1, s57
	v_mov_b32_e32 v70, s18
	s_add_i32 s19, s88, s57
	s_lshl_b32 s45, s8, 2
	ds_read_b128 v[70:73], v70
	v_mov_b32_e32 v74, s19
	s_add_i32 s20, s1, s45
	ds_read_b128 v[116:119], v74
	v_mov_b32_e32 v74, s20
	s_add_i32 s21, s88, s45
	ds_read_b128 v[120:123], v74
	v_mov_b32_e32 v74, s21
	ds_read_b128 v[124:127], v74
	s_waitcnt lgkmcnt(3)
	v_mul_f32_e32 v74, 0, v70
	s_waitcnt lgkmcnt(2)
	v_pk_fma_f32 v[80:81], v[116:117], v[64:65], v[74:75] op_sel_hi:[0,1,0]
	v_pk_mul_f32 v[130:131], v[116:117], v[60:61] op_sel:[1,0]
	v_fmac_f32_e32 v74, v82, v116
	s_waitcnt lgkmcnt(1)
	v_mul_f32_e32 v76, 0, v120
	v_pk_fma_f32 v[80:81], v[80:81], v[70:71], v[130:131] op_sel:[0,1,0]
	v_mul_f32_e32 v130, v114, v117
	s_waitcnt lgkmcnt(0)
	v_pk_fma_f32 v[128:129], v[124:125], v[58:59], v[76:77] op_sel_hi:[0,1,0]
	v_mul_f32_e32 v115, v70, v71
	v_fmac_f32_e32 v130, v74, v71
	v_pk_mul_f32 v[70:71], v[124:125], v[54:55] op_sel:[1,0]
	v_fmac_f32_e32 v76, v113, v124
	v_mul_f32_e32 v74, v120, v121
	v_pk_fma_f32 v[70:71], v[128:129], v[120:121], v[70:71] op_sel:[0,1,0]
	v_mul_f32_e32 v120, v111, v125
	v_pk_mul_f32 v[116:117], v[118:119], v[56:57] op_sel_hi:[0,1]
	v_fmac_f32_e32 v120, v76, v121
	v_mul_f32_e32 v76, v115, v72
	v_pk_fma_f32 v[80:81], v[80:81], v[72:73], v[116:117] op_sel_hi:[1,0,1]
	v_mul_f32_e32 v115, v112, v118
	v_mul_f32_e32 v118, v74, v122
	v_pk_mul_f32 v[116:117], v[126:127], v[50:51] op_sel_hi:[0,1]
	v_mov_b32_e32 v74, v119
	v_fmac_f32_e32 v115, v130, v72
	v_pk_fma_f32 v[70:71], v[70:71], v[122:123], v[116:117] op_sel_hi:[1,0,1]
	v_mov_b32_e32 v72, v73
	v_pk_mul_f32 v[116:117], v[74:75], v[52:53] op_sel_hi:[0,1]
	v_mov_b32_e32 v74, v127
	s_or_b32 s6, s57, 16
	v_pk_fma_f32 v[80:81], v[80:81], v[72:73], v[116:117] op_sel_hi:[1,0,1]
	v_mov_b32_e32 v72, v123
	v_pk_mul_f32 v[116:117], v[74:75], v[46:47] op_sel_hi:[0,1]
	v_mul_f32_e32 v121, v109, v126
	v_mul_f32_e32 v132, v110, v119
	v_pk_fma_f32 v[128:129], v[70:71], v[72:73], v[116:117] op_sel_hi:[1,0,1]
	v_fmac_f32_e32 v121, v120, v122
	v_mul_f32_e32 v76, v76, v73
	v_fmac_f32_e32 v132, v115, v73
	v_mul_f32_e32 v115, v118, v123
	v_mul_f32_e32 v74, v107, v127
	v_fmac_f32_e32 v74, v121, v123
	v_and_b32_e32 v9, 0xffff0000, v9
	s_waitcnt vmcnt(5)
	v_lshlrev_b32_e32 v4, 16, v5
	v_and_b32_e32 v5, 0xffff0000, v5
	s_andn2_b64 vcc, exec, s[16:17]
	s_waitcnt vmcnt(2)
	v_lshlrev_b32_e32 v68, 16, v63
	v_and_b32_e32 v69, 0xffff0000, v63
	global_load_dword v63, v3, s[12:13]
	s_add_i32 s12, s1, s6
	s_add_i32 s13, s88, s6
	s_or_b32 s6, s45, 16
	v_mov_b32_e32 v70, s12
	v_mov_b32_e32 v116, s13
	s_add_i32 s14, s1, s6
	s_add_i32 s15, s88, s6
	ds_read_b128 v[70:73], v70
	ds_read_b128 v[116:119], v116
	v_mov_b32_e32 v120, s14
	v_mov_b32_e32 v124, s15
	ds_read_b128 v[120:123], v120
	ds_read_b128 v[124:127], v124
	s_waitcnt lgkmcnt(2)
	v_pk_mul_f32 v[130:131], v[116:117], v[48:49] op_sel_hi:[0,1]
	v_mul_f32_e32 v133, v108, v116
	v_mul_f32_e32 v76, v76, v70
	v_pk_fma_f32 v[80:81], v[80:81], v[70:71], v[130:131] op_sel_hi:[1,0,1]
	v_fmac_f32_e32 v133, v132, v70
	s_waitcnt lgkmcnt(0)
; __device__ __forceinline__ void ph5_m2(const Frame& F, const Args& A) {
;     ...
; #pragma unroll
;         for (int i = 0; i < 16; ++i) { const float dA = decL[hA * 128 + 16 * g + i], sA = sclL[hA * 128 + 16 * g + i], dB = decL[hB * 128 + 16 * g + i], sB = sclL[hB * 128 + 16 * g + i];
;             ApA *= dA; BpA = BpA * dA + uA[i] * sA; BnA = BnA * dA + nA[i] * sA; ApB *= dB; BpB = BpB * dB + uB[i] * sB; BnB = BnB * dB + nB[i] * sB; }
;         seg[g * 128 + 2 * l] = ApA; seg[1024 + g * 128 + 2 * l] = BpA.x; seg[1024 + g * 128 + 2 * l + 1] = BpA.y; seg[2048 + g * 64 + l] = BnA;
;         seg[3072 + g * 128 + 2 * l] = ApB; seg[3072 + 1024 + g * 128 + 2 * l] = BpB.x; seg[3072 + 1024 + g * 128 + 2 * l + 1] = BpB.y; seg[3072 + 2048 + g * 64 + l] = BnB;
;         __syncthreads();
;         f32x2_t stA = {0.f, 0.f}, stB = {0.f, 0.f}; float snsA = 0.f, snsB = 0.f;
	v_pk_mul_f32 v[130:131], v[124:125], v[42:43] op_sel_hi:[0,1]
	v_mul_f32_e32 v132, v105, v124
	v_pk_fma_f32 v[128:129], v[128:129], v[120:121], v[130:131] op_sel_hi:[1,0,1]
	v_fmac_f32_e32 v132, v74, v120
	v_mul_f32_e32 v74, v76, v71
	v_pk_mul_f32 v[130:131], v[116:117], v[44:45] op_sel:[1,0]
	v_mul_f32_e32 v76, v106, v117
	v_mul_f32_e32 v115, v115, v120
	v_pk_fma_f32 v[80:81], v[80:81], v[70:71], v[130:131] op_sel:[0,1,0]
	v_fmac_f32_e32 v76, v133, v71
	v_pk_mul_f32 v[70:71], v[124:125], v[38:39] op_sel:[1,0]
	v_mul_f32_e32 v74, v74, v72
	v_pk_mul_f32 v[116:117], v[118:119], v[40:41] op_sel_hi:[0,1]
	v_mul_f32_e32 v115, v115, v121
	v_pk_fma_f32 v[70:71], v[128:129], v[120:121], v[70:71] op_sel:[0,1,0]
	v_mul_f32_e32 v120, v103, v125
	v_pk_fma_f32 v[80:81], v[80:81], v[72:73], v[116:117] op_sel_hi:[1,0,1]
	v_mul_f32_e32 v118, v104, v118
	v_pk_mul_f32 v[116:117], v[126:127], v[34:35] op_sel_hi:[0,1]
	v_mul_f32_e32 v130, v74, v73
	v_mov_b32_e32 v74, v119
	v_fmac_f32_e32 v120, v132, v121
	v_fmac_f32_e32 v118, v76, v72
	v_mul_f32_e32 v76, v115, v122
	v_pk_fma_f32 v[70:71], v[70:71], v[122:123], v[116:117] op_sel_hi:[1,0,1]
	v_mul_f32_e32 v115, v101, v126
	v_mov_b32_e32 v72, v73
	v_pk_mul_f32 v[116:117], v[74:75], v[36:37] op_sel_hi:[0,1]
	v_mov_b32_e32 v74, v127
	s_or_b32 s6, s57, 32
	v_fmac_f32_e32 v115, v120, v122
	v_pk_fma_f32 v[80:81], v[80:81], v[72:73], v[116:117] op_sel_hi:[1,0,1]
	v_mov_b32_e32 v72, v123
	v_pk_mul_f32 v[116:117], v[74:75], v[30:31] op_sel_hi:[0,1]
	v_mul_f32_e32 v74, v99, v127
	s_add_i32 s8, s1, s6
	s_add_i32 s9, s88, s6
	s_or_b32 s6, s45, 32
	v_mul_f32_e32 v132, v102, v119
	v_pk_fma_f32 v[128:129], v[70:71], v[72:73], v[116:117] op_sel_hi:[1,0,1]
	v_fmac_f32_e32 v74, v115, v123
	v_mov_b32_e32 v70, s8
	v_mov_b32_e32 v115, s9
	s_add_i32 s10, s1, s6
	v_fmac_f32_e32 v132, v118, v73
	ds_read_b128 v[70:73], v70
	ds_read_b128 v[116:119], v115
	v_mov_b32_e32 v115, s10
	s_add_i32 s11, s88, s6
	v_mul_f32_e32 v76, v76, v123
	ds_read_b128 v[120:123], v115
	v_mov_b32_e32 v115, s11
	ds_read_b128 v[124:127], v115
	s_waitcnt lgkmcnt(3)
	v_mul_f32_e32 v115, v130, v70
	s_waitcnt lgkmcnt(2)
	v_pk_mul_f32 v[130:131], v[116:117], v[32:33] op_sel_hi:[0,1]
	v_mul_f32_e32 v133, v100, v116
	v_pk_fma_f32 v[80:81], v[80:81], v[70:71], v[130:131] op_sel_hi:[1,0,1]
	v_fmac_f32_e32 v133, v132, v70
	s_waitcnt lgkmcnt(0)
	v_pk_mul_f32 v[130:131], v[124:125], v[26:27] op_sel_hi:[0,1]
	v_mul_f32_e32 v132, v97, v124
	v_pk_fma_f32 v[128:129], v[128:129], v[120:121], v[130:131] op_sel_hi:[1,0,1]
	v_fmac_f32_e32 v132, v74, v120
	v_mul_f32_e32 v74, v115, v71
	v_pk_mul_f32 v[130:131], v[116:117], v[28:29] op_sel:[1,0]
	v_mul_f32_e32 v115, v98, v117
	v_pk_fma_f32 v[80:81], v[80:81], v[70:71], v[130:131] op_sel:[0,1,0]
	v_fmac_f32_e32 v115, v133, v71
	v_pk_mul_f32 v[70:71], v[124:125], v[22:23] op_sel:[1,0]
	v_mul_f32_e32 v74, v74, v72
	v_pk_mul_f32 v[116:117], v[118:119], v[24:25] op_sel_hi:[0,1]
	v_mul_f32_e32 v76, v76, v120
	v_pk_fma_f32 v[70:71], v[128:129], v[120:121], v[70:71] op_sel:[0,1,0]
	v_mul_f32_e32 v120, v95, v125
	v_pk_fma_f32 v[80:81], v[80:81], v[72:73], v[116:117] op_sel_hi:[1,0,1]
	v_mul_f32_e32 v118, v96, v118
	v_pk_mul_f32 v[116:117], v[126:127], v[18:19] op_sel_hi:[0,1]
	v_mul_f32_e32 v130, v74, v73
	v_mov_b32_e32 v74, v119
	v_fmac_f32_e32 v120, v132, v121
	v_fmac_f32_e32 v118, v115, v72
	v_pk_fma_f32 v[70:71], v[70:71], v[122:123], v[116:117] op_sel_hi:[1,0,1]
	v_mul_f32_e32 v115, v93, v126
	v_mov_b32_e32 v72, v73
	v_pk_mul_f32 v[116:117], v[74:75], v[20:21] op_sel_hi:[0,1]
	v_mov_b32_e32 v74, v127
	s_or_b32 s6, s57, 48
	v_fmac_f32_e32 v115, v120, v122
	v_pk_fma_f32 v[80:81], v[80:81], v[72:73], v[116:117] op_sel_hi:[1,0,1]
	v_mov_b32_e32 v72, v123
	v_pk_mul_f32 v[116:117], v[74:75], v[14:15] op_sel_hi:[0,1]
	v_mul_f32_e32 v74, v91, v127
	s_add_i32 s46, s1, s6
	s_add_i32 s47, s88, s6
	s_or_b32 s6, s45, 48
	v_mul_f32_e32 v76, v76, v121
	v_mul_f32_e32 v132, v94, v119
	v_pk_fma_f32 v[128:129], v[70:71], v[72:73], v[116:117] op_sel_hi:[1,0,1]
	v_fmac_f32_e32 v74, v115, v123
	v_mov_b32_e32 v70, s46
	v_mov_b32_e32 v115, s47
	s_add_i32 s33, s1, s6
	v_mul_f32_e32 v76, v76, v122
	v_fmac_f32_e32 v132, v118, v73
	ds_read_b128 v[70:73], v70
	ds_read_b128 v[116:119], v115
	v_mov_b32_e32 v115, s33
	s_add_i32 s6, s88, s6
	v_mul_f32_e32 v76, v76, v123
	ds_read_b128 v[120:123], v115
	v_mov_b32_e32 v115, s6
	ds_read_b128 v[124:127], v115
	s_waitcnt lgkmcnt(3)
	v_mul_f32_e32 v115, v130, v70
	s_waitcnt lgkmcnt(2)
	v_pk_mul_f32 v[130:131], v[116:117], v[16:17] op_sel_hi:[0,1]
	v_mul_f32_e32 v133, v92, v116
	v_pk_fma_f32 v[80:81], v[80:81], v[70:71], v[130:131] op_sel_hi:[1,0,1]
	v_fmac_f32_e32 v133, v132, v70
	s_waitcnt lgkmcnt(0)
	v_pk_mul_f32 v[130:131], v[124:125], v[10:11] op_sel_hi:[0,1]
	v_mul_f32_e32 v132, v89, v124
	v_pk_fma_f32 v[128:129], v[128:129], v[120:121], v[130:131] op_sel_hi:[1,0,1]
	v_fmac_f32_e32 v132, v74, v120
	v_mul_f32_e32 v74, v115, v71
	v_pk_mul_f32 v[130:131], v[116:117], v[12:13] op_sel:[1,0]
	v_mul_f32_e32 v115, v90, v117
	v_pk_fma_f32 v[80:81], v[80:81], v[70:71], v[130:131] op_sel:[0,1,0]
	v_fmac_f32_e32 v115, v133, v71
	v_pk_mul_f32 v[70:71], v[124:125], v[6:7] op_sel:[1,0]
	v_pk_mul_f32 v[116:117], v[118:119], v[8:9] op_sel_hi:[0,1]
	v_mul_f32_e32 v76, v76, v120
	v_pk_fma_f32 v[70:71], v[128:129], v[120:121], v[70:71] op_sel:[0,1,0]
	v_mul_f32_e32 v74, v74, v72
	v_pk_fma_f32 v[80:81], v[80:81], v[72:73], v[116:117] op_sel_hi:[1,0,1]
	v_pk_mul_f32 v[116:117], v[126:127], v[4:5] op_sel_hi:[0,1]
	v_mul_f32_e32 v76, v76, v121
	v_mul_f32_e32 v118, v87, v118
	v_pk_fma_f32 v[70:71], v[70:71], v[122:123], v[116:117] op_sel_hi:[1,0,1]
	v_mul_f32_e32 v116, v74, v73
	v_mov_b32_e32 v74, v119
	s_waitcnt vmcnt(2)
	v_lshlrev_b32_e32 v66, 16, v67
	v_and_b32_e32 v67, 0xffff0000, v67
	v_mul_f32_e32 v120, v88, v125
	v_fmac_f32_e32 v118, v115, v72
	v_mul_f32_e32 v76, v76, v122
	v_mov_b32_e32 v72, v73
	v_pk_mul_f32 v[68:69], v[74:75], v[68:69] op_sel_hi:[0,1]
	s_waitcnt vmcnt(0)
	v_mul_f32_e32 v63, v63, v119
	v_mov_b32_e32 v74, v127
	v_fmac_f32_e32 v120, v132, v121
	v_mul_f32_e32 v115, v86, v126
	v_pk_fma_f32 v[68:69], v[80:81], v[72:73], v[68:69] op_sel_hi:[1,0,1]
	v_fmac_f32_e32 v63, v118, v73
	v_mul_f32_e32 v73, v76, v123
	v_mov_b32_e32 v72, v123
	v_pk_mul_f32 v[66:67], v[74:75], v[66:67] op_sel_hi:[0,1]
	v_fmac_f32_e32 v115, v120, v122
	v_pk_fma_f32 v[66:67], v[70:71], v[72:73], v[66:67] op_sel_hi:[1,0,1]
	v_mul_f32_e32 v70, v78, v127
	v_fmac_f32_e32 v70, v115, v123
	ds_write_b32 v77, v116
	ds_write_b64 v77, v[68:69] offset:4096
	ds_write_b32 v79, v63 offset:8192
	ds_write_b32 v77, v73 offset:12288
	ds_write_b64 v77, v[66:67] offset:16384
	ds_write_b32 v79, v70 offset:20480
	v_mov_b32_e32 v69, 0
	v_mov_b32_e32 v68, 0
	v_mov_b32_e32 v71, 0
	v_mov_b32_e32 v70, 0
	v_mov_b32_e32 v73, 0
	v_mov_b32_e32 v72, 0
	s_waitcnt lgkmcnt(0)
	s_barrier
; __device__ __forceinline__ void ph5_m2(const Frame& F, const Args& A) {
;     ...
;         f32x2_t stA = {0.f, 0.f}, stB = {0.f, 0.f}; float snsA = 0.f, snsB = 0.f;
;         for (int q = 0; q < g; ++q) { const float a = seg[q * 128 + 2 * l], b = seg[3072 + q * 128 + 2 * l];
;             stA.x = stA.x * a + seg[1024 + q * 128 + 2 * l]; stA.y = stA.y * a + seg[1024 + q * 128 + 2 * l + 1]; snsA = snsA * a + seg[2048 + q * 64 + l];
;             stB.x = stB.x * b + seg[3072 + 1024 + q * 128 + 2 * l]; stB.y = stB.y * b + seg[3072 + 1024 + q * 128 + 2 * l + 1]; snsB = snsB * b + seg[3072 + 2048 + q * 64 + l]; }
	s_cbranch_vccnz .LBB0_592
	v_readlane_b32 s16, v254, 50
	v_readlane_b32 s17, v254, 51
	s_andn2_b64 vcc, exec, s[16:17]
	s_cbranch_vccnz .LBB0_588
	v_mov_b32_e32 v70, 0
	s_mov_b32 s16, 0
	v_mov_b32_e32 v63, v84
	v_mov_b32_e32 v66, v83
	v_mov_b32_e32 v71, v70
	v_mov_b32_e32 v72, v70
	v_mov_b32_e32 v73, v70
	v_mov_b32_e32 v68, v70
	v_mov_b32_e32 v69, v70

; __device__ __forceinline__ void ph6_unit(const Frame& F, const Args& A, int c, int h) {
;     ...
;         const v4u* Qg = (const v4u*)((const bf16*)(ws + WS_QM) + ((size_t)h * S_ + t0) * 64); const v4u* Kg = (const v4u*)((const bf16*)(ws + WS_KM) + ((size_t)h * S_ + t0) * 64);
;         const v4u* Cg = (const v4u*)((const bf16*)(ws + WS_CST) + ((size_t)h * 128 + c) * 8192);
;         const v4u q4 = Qg[tid], k4 = Kg[tid], c40 = Cg[tid], c41 = Cg[tid + 512];
;         v4u vv[2];
; #pragma unroll
;         for (int i = 0; i < 2; ++i) { const int idx = tid + 512 * i, sx = idx >> 4, c8 = (idx & 15) * 8; vv[i] = *(const v4u*)(Z + (size_t)(t0 + sx) * pg8::ZLD + 1024 + h * 128 + c8); }
;         const float mprev = ((const float*)(ws + WS_SC))[3072 + h * 128 + c];
;         if (F.wave == 0) { const float b = ((const float*)(ws + WS_BL))[h * S_ + t0 + lane], ip = ((const float*)(ws + WS_IPL))[h * S_ + t0 + lane];
;             const float pm = wave_scan_max(ip - b, lane); const float mt = b + fmaxf(mprev, pm);
;             mtL[lane] = mt; wiL[lane] = expf(b + mprev - mt); btm[lane] = b - mt; ibs[lane] = ip - b;
;             nL[lane] = ((const float*)(ws + WS_NST))[((size_t)h * 128 + c) * 64 + lane]; }
.LBB0_942:
	s_ashr_i32 s80, s89, 3
	s_lshl_b32 s0, s80, 6
	s_and_b32 s77, s89, 7
	s_ashr_i32 s1, s0, 31
	s_lshl_b32 s54, s77, 19
	s_lshl_b64 s[50:51], s[0:1], 6
	s_add_u32 s84, s50, s54
	s_addc_u32 s85, s51, 0
	s_ashr_i32 s1, s80, 31
	s_lshl_b32 s96, s77, 7
	s_add_u32 s50, s96, s80
	s_addc_u32 s51, 0, s1
	s_lshl_b64 s[84:85], s[84:85], 1
	v_add_u32_e32 v18, s0, v35
	s_lshl_b64 s[90:91], s[50:51], 14
	v_lshl_add_u64 v[2:3], v[40:41], 0, s[84:85]
	v_lshl_add_u64 v[6:7], v[42:43], 0, s[84:85]
	v_mad_i64_i32 v[18:19], s[84:85], v18, s88, v[56:57]
	v_lshl_add_u64 v[10:11], v[44:45], 0, s[90:91]
	s_movk_i32 s1, 0x2000
	s_lshl_b32 s84, s77, 8
	s_mov_b32 s85, s97
	v_add_co_u32_e32 v14, vcc, s1, v10
	v_lshl_add_u64 v[18:19], v[18:19], 0, s[84:85]
	v_add_u32_e32 v20, s0, v39
	v_addc_co_u32_e32 v15, vcc, 0, v11, vcc
	v_lshl_add_u64 v[18:19], v[18:19], 0, v[46:47]
	s_mov_b32 s1, 0x17e00000
	v_mad_i64_i32 v[20:21], s[90:91], v20, s88, v[56:57]
	v_add_co_u32_e32 v18, vcc, s1, v18
	v_lshl_add_u64 v[20:21], v[20:21], 0, s[84:85]
	s_nop 0
	v_addc_co_u32_e32 v19, vcc, 0, v19, vcc
	v_lshl_add_u64 v[20:21], v[20:21], 0, v[46:47]
	v_add_co_u32_e32 v22, vcc, 0x17e00000, v20
	global_load_dwordx4 v[2:5], v[2:3], off
	s_nop 0
	global_load_dwordx4 v[6:9], v[6:7], off
	v_addc_co_u32_e32 v23, vcc, 0, v21, vcc
	global_load_dwordx4 v[10:13], v[10:11], off
	s_nop 0
	global_load_dwordx4 v[14:17], v[14:15], off
	s_nop 0
	global_load_dwordx4 v[18:21], v[18:19], off offset:2048
	s_nop 0
	global_load_dwordx4 v[22:25], v[22:23], off offset:2048
	s_andn2_b64 vcc, exec, s[2:3]
	s_cbranch_vccnz .LBB0_944
	s_add_i32 s1, s80, s96
	s_add_i32 s80, s1, 0xc00
	s_ashr_i32 s81, s80, 31
	s_lshl_b64 s[80:81], s[80:81], 2
	s_add_u32 s80, s33, s80
	s_addc_u32 s81, s86, s81
	s_lshl_b32 s1, s77, 13
	s_add_i32 s1, s1, s0
	v_or_b32_e32 v26, s1, v1
	v_ashrrev_i32_e32 v27, 31, v26
	v_lshlrev_b64 v[26:27], 2, v[26:27]
	v_lshl_add_u64 v[28:29], s[4:5], 0, v[26:27]
	v_lshl_add_u64 v[26:27], s[6:7], 0, v[26:27]
	global_load_dword v30, v47, s[80:81]
	v_add_u32_e32 v31, -2, v76
	global_load_dword v28, v[28:29], off
	s_mov_b32 s1, 0x3fb8aa3b
	global_load_dword v26, v[26:27], off
	v_and_b32_e32 v27, 64, v76
	v_add_u32_e32 v29, -1, v76
	v_cmp_lt_i32_e32 vcc, v29, v27
	s_lshl_b64 s[50:51], s[50:51], 8
	v_lshl_add_u64 v[116:117], v[48:49], 0, s[50:51]
	global_load_dword v118, v[116:117], off
	s_waitcnt vmcnt(0)
	v_sub_f32_e32 v26, v26, v28
	v_cndmask_b32_e32 v29, v29, v76, vcc
	v_lshlrev_b32_e32 v29, 2, v29
	ds_bpermute_b32 v29, v29, v26
	v_cmp_lt_i32_e32 vcc, v31, v27
	s_waitcnt lgkmcnt(0)
	v_max_f32_e32 v29, v29, v29
	v_max_f32_e32 v29, v26, v29
	v_cndmask_b32_e32 v31, v31, v76, vcc
	v_cndmask_b32_e64 v29, v29, v26, s[52:53]
	v_lshlrev_b32_e32 v31, 2, v31
	ds_bpermute_b32 v31, v31, v29
	s_waitcnt lgkmcnt(0)
	v_max_f32_e32 v31, v31, v31
	v_max_f32_e32 v31, v29, v31
	v_cndmask_b32_e64 v29, v31, v29, s[58:59]
	v_add_u32_e32 v31, -4, v76
	v_cmp_lt_i32_e32 vcc, v31, v27
	s_nop 1
	v_cndmask_b32_e32 v31, v31, v76, vcc
	v_lshlrev_b32_e32 v31, 2, v31
	ds_bpermute_b32 v31, v31, v29
	s_waitcnt lgkmcnt(0)
	v_max_f32_e32 v31, v31, v31
	v_max_f32_e32 v31, v29, v31
	v_cndmask_b32_e64 v29, v31, v29, s[60:61]
	v_add_u32_e32 v31, -8, v76
	v_cmp_lt_i32_e32 vcc, v31, v27
	s_nop 1
	v_cndmask_b32_e32 v31, v31, v76, vcc
	v_lshlrev_b32_e32 v31, 2, v31
	ds_bpermute_b32 v31, v31, v29
	s_waitcnt lgkmcnt(0)
	v_max_f32_e32 v31, v31, v31
	v_max_f32_e32 v31, v29, v31
	v_cndmask_b32_e64 v29, v31, v29, s[62:63]
	v_add_u32_e32 v31, -16, v76
	v_cmp_lt_i32_e32 vcc, v31, v27
	s_nop 1
	v_cndmask_b32_e32 v31, v31, v76, vcc
	v_lshlrev_b32_e32 v31, 2, v31
	ds_bpermute_b32 v31, v31, v29
	s_waitcnt lgkmcnt(0)
	v_max_f32_e32 v31, v31, v31
	v_max_f32_e32 v31, v29, v31
	v_cndmask_b32_e64 v29, v31, v29, s[64:65]
	v_subrev_u32_e32 v31, 32, v76
	v_cmp_lt_i32_e32 vcc, v31, v27
	s_nop 1
	v_cndmask_b32_e32 v27, v31, v76, vcc
	v_lshlrev_b32_e32 v27, 2, v27
	ds_bpermute_b32 v27, v27, v29
	v_max_f32_e32 v31, v29, v29
	s_waitcnt lgkmcnt(0)
	v_max_f32_e32 v27, v27, v27
	v_max_f32_e32 v27, v31, v27
	v_cndmask_b32_e64 v27, v27, v29, s[12:13]
	v_max_f32_e32 v27, v27, v27
	v_max_f32_e32 v29, v30, v30
	v_max_f32_e32 v27, v29, v27
	v_add_f32_e32 v27, v28, v27
	v_add_f32_e32 v29, v30, v28
	v_sub_f32_e32 v29, v29, v27
	v_mul_f32_e32 v30, 0x3fb8aa3b, v29
	v_fma_f32 v31, v29, s1, -v30
	v_rndne_f32_e32 v32, v30
	v_fmac_f32_e32 v31, 0x32a5705f, v29
	v_sub_f32_e32 v30, v30, v32
	v_add_f32_e32 v30, v30, v31
	v_exp_f32_e32 v30, v30
	v_cvt_i32_f32_e32 v31, v32
	s_mov_b32 s1, 0xc2ce8ed0
	v_cmp_ngt_f32_e32 vcc, s1, v29
	s_mov_b32 s1, 0x42b17218
	v_ldexp_f32 v30, v30, v31
	v_cndmask_b32_e32 v30, 0, v30, vcc
	v_cmp_nlt_f32_e32 vcc, s1, v29
	s_nop 1
	v_cndmask_b32_e32 v29, v79, v30, vcc
	ds_write2st64_b32 v62, v27, v29 offset0:246 offset1:247
	v_sub_f32_e32 v27, v28, v27
	ds_write2st64_b32 v62, v27, v26 offset0:244 offset1:245
	v_mov_b32_e32 v26, v118
	ds_write_b32 v62, v26 offset:63488

;     __device__ __forceinline__ void operator()(const f32x4 (&acc)[2][2][4][2], const Unit& u, int wr, int wc, int fr, int fq) const {
;     ...
;         const int e = u.pn >> 4, j = u.pn & 15, colL = 128 * j + wc * 32 + 8 * fq, row0 = u.pm * HALF + wr * 64 + fr;
;         f32x4 bg[2], bu[2];
; #pragma unroll
;         for (int n = 0; n < 2; ++n) { bg[n] = *(const f32x4*)(bgu + (size_t)e * 4096 + colL + 4 * n); bu[n] = *(const f32x4*)(bgu + (size_t)e * 4096 + 2048 + colL + 4 * n); }
; template <class Epi, class Sched, bool ALIGN_EPI = false, bool SP2 = false, bool FP8 = false>
; __device__ __forceinline__ void gemm_phase(PG8_LAS unsigned char* lds, const Gemm g, const Sched& S, const Epi& E) {
;     ...
;         for (int a = 0; a < 2; ++a)
; #pragma unroll
;             for (int b = 0; b < 2; ++b)
; #pragma unroll
;                 for (int m = 0; m < 4; ++m)
; #pragma unroll
;                     for (int n = 0; n < 2; ++n) acc[a][b][m][n] = (f32x4){0.f, 0.f, 0.f, 0.f};
;         cur = nxt; cA = nA; cB = nB; ++ui;
.LBB0_1340:
	s_ashr_i32 s21, s20, 31
	s_lshl_b64 s[24:25], s[20:21], 18
	s_add_u32 s24, s42, s24
	s_addc_u32 s25, s43, s25
	s_and_b64 s[28:29], s[26:27], exec
	s_cselect_b32 s21, s25, s37
	s_cselect_b32 s72, s24, s36
	s_ashr_i32 s23, s22, 31
	s_lshl_b64 s[28:29], s[22:23], 19
	s_add_u32 s28, s44, s28
	s_addc_u32 s29, s45, s29
	s_and_b64 s[34:35], s[26:27], exec
	s_cselect_b32 s23, s29, s3
	s_cselect_b32 s73, s28, s2
	s_cmp_eq_u32 s38, 0
	s_cselect_b64 s[34:35], -1, 0
	s_add_u32 s36, s36, 0x40080
	s_addc_u32 s37, s37, 0
	v_mov_b32_e32 v68, v66
	v_mov_b32_e32 v69, v66
	s_add_u32 s74, s2, 0x100
	v_mov_b32_e32 v67, v66
	v_mov_b32_e32 v134, 0
	v_mov_b64_e32 v[72:73], v[68:69]
	v_mov_b64_e32 v[80:81], v[68:69]
	v_mov_b64_e32 v[88:89], v[68:69]
	v_mov_b64_e32 v[96:97], v[68:69]
	v_mov_b64_e32 v[104:105], v[68:69]
	v_mov_b64_e32 v[112:113], v[68:69]
	v_mov_b64_e32 v[120:121], v[68:69]
	v_mov_b64_e32 v[128:129], v[68:69]
	v_mov_b64_e32 v[76:77], v[68:69]
	v_mov_b64_e32 v[84:85], v[68:69]
	v_mov_b64_e32 v[92:93], v[68:69]
	v_mov_b64_e32 v[100:101], v[68:69]
	v_mov_b64_e32 v[108:109], v[68:69]
	v_mov_b64_e32 v[116:117], v[68:69]
	v_mov_b64_e32 v[124:125], v[68:69]
	v_mov_b64_e32 v[132:133], v[68:69]
	s_addc_u32 s75, s3, 0
	s_mov_b32 s76, -2
	v_cndmask_b32_e64 v222, 0, 1, s[34:35]
	v_mov_b64_e32 v[70:71], v[66:67]
	v_mov_b64_e32 v[78:79], v[66:67]
	v_mov_b64_e32 v[86:87], v[66:67]
	v_mov_b64_e32 v[94:95], v[66:67]
	v_mov_b64_e32 v[102:103], v[66:67]
	v_mov_b64_e32 v[110:111], v[66:67]
	v_mov_b64_e32 v[118:119], v[66:67]
	v_mov_b64_e32 v[126:127], v[66:67]
	v_mov_b64_e32 v[74:75], v[66:67]
	v_mov_b64_e32 v[82:83], v[66:67]
	v_mov_b64_e32 v[90:91], v[66:67]
	v_mov_b64_e32 v[98:99], v[66:67]
	v_mov_b64_e32 v[106:107], v[66:67]
	v_mov_b64_e32 v[114:115], v[66:67]
	v_mov_b64_e32 v[122:123], v[66:67]
	v_mov_b64_e32 v[130:131], v[66:67]
	v_mov_b32_e32 v135, v134
	v_mov_b32_e32 v136, v134
	v_mov_b32_e32 v137, v134
	v_mov_b32_e32 v142, v134
	v_mov_b32_e32 v143, v134
	v_mov_b32_e32 v144, v134
	v_mov_b32_e32 v145, v134
	v_mov_b32_e32 v150, v134
	v_mov_b32_e32 v151, v134
	v_mov_b32_e32 v152, v134
	v_mov_b32_e32 v153, v134
	v_mov_b32_e32 v158, v134
	v_mov_b32_e32 v159, v134
	v_mov_b32_e32 v160, v134
	v_mov_b32_e32 v161, v134
	v_mov_b32_e32 v166, v134
	v_mov_b32_e32 v167, v134
	v_mov_b32_e32 v168, v134
	v_mov_b32_e32 v169, v134
	v_mov_b32_e32 v174, v134
	v_mov_b32_e32 v175, v134
	v_mov_b32_e32 v176, v134
	v_mov_b32_e32 v177, v134
	v_mov_b32_e32 v182, v134
	v_mov_b32_e32 v183, v134
	v_mov_b32_e32 v184, v134
	v_mov_b32_e32 v185, v134
	v_mov_b32_e32 v190, v134
	v_mov_b32_e32 v191, v134
	v_mov_b32_e32 v192, v134
	v_mov_b32_e32 v193, v134
	v_mov_b32_e32 v138, v134
	v_mov_b32_e32 v139, v134
	v_mov_b32_e32 v140, v134
	v_mov_b32_e32 v141, v134
	v_mov_b32_e32 v146, v134
	v_mov_b32_e32 v147, v134
	v_mov_b32_e32 v148, v134
	v_mov_b32_e32 v149, v134
	v_mov_b32_e32 v154, v134
	v_mov_b32_e32 v155, v134
	v_mov_b32_e32 v156, v134
	v_mov_b32_e32 v157, v134
	v_mov_b32_e32 v162, v134
	v_mov_b32_e32 v163, v134
	v_mov_b32_e32 v164, v134
	v_mov_b32_e32 v165, v134
	v_mov_b32_e32 v170, v134
	v_mov_b32_e32 v171, v134
	v_mov_b32_e32 v172, v134
	v_mov_b32_e32 v173, v134
	v_mov_b32_e32 v178, v134
	v_mov_b32_e32 v179, v134
	v_mov_b32_e32 v180, v134
	v_mov_b32_e32 v181, v134
	v_mov_b32_e32 v186, v134
	v_mov_b32_e32 v187, v134
	v_mov_b32_e32 v188, v134
	v_mov_b32_e32 v189, v134
	v_mov_b32_e32 v194, v134
	v_mov_b32_e32 v195, v134
	v_mov_b32_e32 v196, v134
	v_mov_b32_e32 v197, v134
	v_mov_b32_e32 v242, s30
	v_ashrrev_i32_e32 v243, 4, v242
	v_and_b32_e32 v242, 15, v242
	v_lshlrev_b32_e32 v242, 7, v242
	v_or_b32_e32 v242, s54, v242
	v_lshl_add_u32 v242, v216, 3, v242
	v_lshlrev_b32_e32 v242, 2, v242
	v_lshl_add_u32 v242, v243, 14, v242
	v_add_u32_e32 v243, 0x2000, v242
	global_load_dwordx4 v[226:229], v242, s[78:79]
	global_load_dwordx4 v[230:233], v242, s[78:79] offset:16
	global_load_dwordx4 v[234:237], v243, s[78:79]
	global_load_dwordx4 v[238:241], v243, s[78:79] offset:16
	s_branch .LBB0_1342

; __device__ __forceinline__ float sigmoidf_(float x) { return __builtin_amdgcn_rcpf(1.f + __builtin_amdgcn_exp2f(-1.4426950408889634f * x)); }
; __device__ __forceinline__ unsigned pack_fp8x4(float a, float b, float c, float d) { int w = __builtin_amdgcn_cvt_pk_fp8_f32(a, b, 0, false); w = __builtin_amdgcn_cvt_pk_fp8_f32(c, d, w, true); return (unsigned)w; }
; #define ACT(t) (KBASE(t) <= qlo + QBLK - 1 && KBASE(t) + KVBLK - 1 >= qlo - W + 1)
;     __device__ __forceinline__ void operator()(const f32x4 (&acc)[2][2][4][2], const Unit& u, int wr, int wc, int fr, int fq) const {
;         asm volatile("" : "+v"(fr), "+v"(fq));
;         const int e = u.pn >> 4, j = u.pn & 15, colL = 128 * j + wc * 32 + 8 * fq, row0 = u.pm * HALF + wr * 64 + fr;
;         f32x4 bg[2], bu[2];
; #pragma unroll
;         for (int n = 0; n < 2; ++n) { bg[n] = *(const f32x4*)(bgu + (size_t)e * 4096 + colL + 4 * n); bu[n] = *(const f32x4*)(bgu + (size_t)e * 4096 + 2048 + colL + 4 * n); }
; #pragma unroll
;         for (int ai = 0; ai < 2; ++ai) if (!(ai == 1 && u.half))
; #pragma unroll
;             for (int m = 0; m < 4; ++m) { const size_t row = (size_t)(row0 + ai * HALF + m * 16);
;                 float a[8];
; #pragma unroll
;                 for (int n = 0; n < 2; ++n)
; #pragma unroll
;                     for (int i = 0; i < 4; ++i) { float g = acc[ai][0][m][n][i] * 0.015625f + bg[n][i], up = acc[ai][1][m][n][i] * 0.015625f + bu[n][i];
;                         g = fminf(g, 7.0f); up = fminf(fmaxf(up, -7.0f), 7.0f);
;                         a[4 * n + i] = (up + 1.0f) * g * sigmoidf_(1.702f * g); }
;                 uint2 w; w.x = pack_fp8x4(a[0], a[1], a[2], a[3]); w.y = pack_fp8x4(a[4], a[5], a[6], a[7]);
;                 *(uint2*)(ACT + row * 2048 + colL) = w; }
.LBB0_1352:
	s_ashr_i32 s34, s30, 4
	s_lshl_b32 s21, s30, 7
	s_and_b32 s21, s21, 0x780
	s_ashr_i32 s35, s34, 31
	v_mov_b32_e32 v2, v216
	v_mov_b32_e32 v20, v1
	s_or_b32 s21, s21, s54
	s_lshl_b64 s[34:35], s[34:35], 14
	s_nop 15
	s_nop 15
	s_add_u32 s34, s78, s34
	v_lshl_add_u32 v18, v2, 3, s21
	s_addc_u32 s35, s79, s35
	v_ashrrev_i32_e32 v19, 31, v18
	v_lshl_add_u64 v[6:7], v[18:19], 2, s[34:35]
	s_movk_i32 s21, 0x2000
	v_add_co_u32_e32 v8, vcc, s21, v6
	v_mov_b64_e32 v[14:15], v[226:227]
	v_mov_b64_e32 v[16:17], v[228:229]
	v_mov_b64_e32 v[2:3], v[230:231]
	v_mov_b64_e32 v[4:5], v[232:233]
	v_addc_co_u32_e32 v9, vcc, 0, v7, vcc
	v_mov_b64_e32 v[10:11], v[234:235]
	v_mov_b64_e32 v[12:13], v[236:237]
	v_lshl_add_u64 v[6:7], v[6:7], 0, s[18:19]
	v_mov_b64_e32 v[6:7], v[238:239]
	v_mov_b64_e32 v[8:9], v[240:241]
	s_lshl_b32 s21, s71, 7
	s_add_i32 s21, s21, s53
	v_add_u32_e32 v20, s21, v20
	s_and_b64 vcc, exec, s[2:3]
	v_fmamk_f32 v21, v194, 0x3c800000, v14
	v_fmamk_f32 v22, v195, 0x3c800000, v15
	v_min_f32_e32 v21, 0x40e00000, v21
	v_min_f32_e32 v22, 0x40e00000, v22
	v_fmamk_f32 v28, v190, 0x3c800000, v10
	v_fmamk_f32 v29, v191, 0x3c800000, v11
	v_med3_f32 v28, v28, s68, v221
	s_waitcnt lgkmcnt(0)
	v_mul_f32_e32 v34, 0x3fd9db23, v21
	v_med3_f32 v29, v29, s68, v221
	v_mul_f32_e32 v35, 0x3fd9db23, v22
	v_add_f32_e32 v28, 1.0, v28
	v_mul_f32_e32 v34, 0xbfb8aa3b, v34
	v_add_f32_e32 v29, 1.0, v29
	v_mul_f32_e32 v35, 0xbfb8aa3b, v35
	v_mul_f32_e32 v21, v21, v28
	v_exp_f32_e32 v28, v34
	v_mul_f32_e32 v22, v22, v29
	v_exp_f32_e32 v29, v35
	v_fmamk_f32 v23, v196, 0x3c800000, v16
	v_fmamk_f32 v26, v187, 0x3c800000, v3
	v_fmamk_f32 v30, v192, 0x3c800000, v12
	v_min_f32_e32 v23, 0x40e00000, v23
	v_min_f32_e32 v26, 0x40e00000, v26
	v_med3_f32 v30, v30, s68, v221
	v_mul_f32_e32 v36, 0x3fd9db23, v23
	v_mul_f32_e32 v39, 0x3fd9db23, v26
	v_add_f32_e32 v30, 1.0, v30
	v_mul_f32_e32 v36, 0xbfb8aa3b, v36
	v_add_f32_e32 v28, 1.0, v28
	v_add_f32_e32 v29, 1.0, v29
	v_mul_f32_e32 v39, 0xbfb8aa3b, v39
	v_mul_f32_e32 v23, v23, v30
	v_exp_f32_e32 v30, v36
	v_rcp_f32_e32 v28, v28
	v_rcp_f32_e32 v29, v29
	v_fmamk_f32 v27, v188, 0x3c800000, v4
	v_exp_f32_e32 v34, v39
	v_min_f32_e32 v27, 0x40e00000, v27
	v_mul_f32_e32 v40, 0x3fd9db23, v27
	v_add_f32_e32 v30, 1.0, v30
	v_mul_f32_e32 v21, v21, v28
	v_mul_f32_e32 v28, v22, v29
	v_mul_f32_e32 v22, 0xbfb8aa3b, v40
	v_add_f32_e32 v34, 1.0, v34
	v_rcp_f32_e32 v30, v30
	v_exp_f32_e32 v22, v22
	v_fmamk_f32 v33, v183, 0x3c800000, v7
	v_rcp_f32_e32 v34, v34
	v_med3_f32 v33, v33, s68, v221
	v_add_f32_e32 v33, 1.0, v33
	v_fmamk_f32 v24, v197, 0x3c800000, v17
	v_mul_f32_e32 v29, v23, v30
	v_mul_f32_e32 v23, v26, v33
	v_add_f32_e32 v22, 1.0, v22
	v_fmamk_f32 v25, v186, 0x3c800000, v2
	v_fmamk_f32 v31, v193, 0x3c800000, v13
	v_min_f32_e32 v24, 0x40e00000, v24
	v_mul_f32_e32 v26, v23, v34
	v_fmamk_f32 v23, v184, 0x3c800000, v8
	v_rcp_f32_e32 v22, v22
	v_fmamk_f32 v32, v182, 0x3c800000, v6
	v_min_f32_e32 v25, 0x40e00000, v25
	v_med3_f32 v31, v31, s68, v221
	v_mul_f32_e32 v37, 0x3fd9db23, v24
	v_med3_f32 v23, v23, s68, v221
	v_med3_f32 v32, v32, s68, v221
	v_mul_f32_e32 v38, 0x3fd9db23, v25
	v_add_f32_e32 v31, 1.0, v31
	v_mul_f32_e32 v37, 0xbfb8aa3b, v37
	v_add_f32_e32 v23, 1.0, v23
	v_add_f32_e32 v32, 1.0, v32
	v_mul_f32_e32 v38, 0xbfb8aa3b, v38
	v_mul_f32_e32 v24, v24, v31
	v_exp_f32_e32 v31, v37
	v_mul_f32_e32 v23, v27, v23
	v_mul_f32_e32 v25, v25, v32
	v_exp_f32_e32 v32, v38
	v_mul_f32_e32 v27, v23, v22
	v_fmamk_f32 v22, v189, 0x3c800000, v5
	v_min_f32_e32 v22, 0x40e00000, v22
	v_mul_f32_e32 v30, 0x3fd9db23, v22
	v_add_f32_e32 v31, 1.0, v31
	v_mul_f32_e32 v30, 0xbfb8aa3b, v30
	v_add_f32_e32 v32, 1.0, v32
	v_rcp_f32_e32 v31, v31
	v_exp_f32_e32 v30, v30
	v_rcp_f32_e32 v32, v32
	v_fmamk_f32 v23, v185, 0x3c800000, v9
	v_med3_f32 v23, v23, s68, v221
	v_add_f32_e32 v23, 1.0, v23
	v_mul_f32_e32 v24, v24, v31
	v_mul_f32_e32 v31, v22, v23
	v_add_f32_e32 v22, 1.0, v30
	v_mul_f32_e32 v25, v25, v32
	v_rcp_f32_e32 v30, v22
	v_mov_b32_e32 v22, 0
	v_mov_b32_e32 v23, 0
	v_cvt_pk_fp8_f32 v22, v21, v28
	v_cvt_pk_fp8_f32 v23, v25, v26
	v_mul_f32_e32 v25, v31, v30
	v_ashrrev_i32_e32 v21, 31, v20
	v_cvt_pk_fp8_f32 v22, v29, v24 op_sel:[0,0,1]
	v_cvt_pk_fp8_f32 v23, v27, v25 op_sel:[0,0,1]
	v_lshlrev_b64 v[24:25], 11, v[20:21]
	v_fmamk_f32 v21, v178, 0x3c800000, v14
	v_min_f32_e32 v21, 0x40e00000, v21
	v_mul_f32_e32 v26, 0x3fd9db23, v21
	v_mul_f32_e32 v26, 0xbfb8aa3b, v26
	v_exp_f32_e32 v26, v26
	v_lshl_add_u64 v[24:25], s[6:7], 0, v[24:25]
	v_lshl_add_u64 v[24:25], v[24:25], 0, v[18:19]
	global_store_dwordx2 v[24:25], v[22:23], off
	v_fmamk_f32 v23, v174, 0x3c800000, v10
	v_add_f32_e32 v24, 1.0, v26
	v_rcp_f32_e32 v24, v24
	v_med3_f32 v23, v23, s68, v221
	v_add_f32_e32 v23, 1.0, v23
	v_mul_f32_e32 v21, v21, v23
	v_fmamk_f32 v23, v179, 0x3c800000, v15
	v_min_f32_e32 v23, 0x40e00000, v23
	v_mul_f32_e32 v21, v21, v24
	v_mul_f32_e32 v24, 0x3fd9db23, v23
	v_mul_f32_e32 v24, 0xbfb8aa3b, v24
	v_exp_f32_e32 v24, v24
	v_fmamk_f32 v26, v180, 0x3c800000, v16
	v_min_f32_e32 v26, 0x40e00000, v26
	v_mul_f32_e32 v27, 0x3fd9db23, v26
	v_mul_f32_e32 v27, 0xbfb8aa3b, v27
	v_add_f32_e32 v24, 1.0, v24
	v_exp_f32_e32 v27, v27
	v_fmamk_f32 v25, v175, 0x3c800000, v11
	v_rcp_f32_e32 v24, v24
	v_med3_f32 v25, v25, s68, v221
	v_add_f32_e32 v25, 1.0, v25
	v_mul_f32_e32 v23, v23, v25
	v_add_f32_e32 v25, 1.0, v27
	v_mul_f32_e32 v23, v23, v24
	v_fmamk_f32 v24, v176, 0x3c800000, v12
	v_rcp_f32_e32 v25, v25
	v_med3_f32 v24, v24, s68, v221
	v_add_f32_e32 v24, 1.0, v24
	v_mul_f32_e32 v24, v26, v24
	v_mul_f32_e32 v26, v24, v25
	v_fmamk_f32 v24, v181, 0x3c800000, v17
	v_min_f32_e32 v24, 0x40e00000, v24
; __device__ __forceinline__ float sigmoidf_(float x) { return __builtin_amdgcn_rcpf(1.f + __builtin_amdgcn_exp2f(-1.4426950408889634f * x)); }
; __device__ __forceinline__ unsigned pack_fp8x4(float a, float b, float c, float d) { int w = __builtin_amdgcn_cvt_pk_fp8_f32(a, b, 0, false); w = __builtin_amdgcn_cvt_pk_fp8_f32(c, d, w, true); return (unsigned)w; }
; #define ACT(t) (KBASE(t) <= qlo + QBLK - 1 && KBASE(t) + KVBLK - 1 >= qlo - W + 1)
;     __device__ __forceinline__ void operator()(const f32x4 (&acc)[2][2][4][2], const Unit& u, int wr, int wc, int fr, int fq) const {
;     ...
;             for (int m = 0; m < 4; ++m) { const size_t row = (size_t)(row0 + ai * HALF + m * 16);
;                 float a[8];
; #pragma unroll
;                 for (int n = 0; n < 2; ++n)
; #pragma unroll
;                     for (int i = 0; i < 4; ++i) { float g = acc[ai][0][m][n][i] * 0.015625f + bg[n][i], up = acc[ai][1][m][n][i] * 0.015625f + bu[n][i];
;                         g = fminf(g, 7.0f); up = fminf(fmaxf(up, -7.0f), 7.0f);
;                         a[4 * n + i] = (up + 1.0f) * g * sigmoidf_(1.702f * g); }
;                 uint2 w; w.x = pack_fp8x4(a[0], a[1], a[2], a[3]); w.y = pack_fp8x4(a[4], a[5], a[6], a[7]);
;                 *(uint2*)(ACT + row * 2048 + colL) = w; }
	v_mul_f32_e32 v25, 0x3fd9db23, v24
	v_mul_f32_e32 v25, 0xbfb8aa3b, v25
	v_exp_f32_e32 v25, v25
	v_fmamk_f32 v28, v170, 0x3c800000, v2
	v_min_f32_e32 v28, 0x40e00000, v28
	v_mul_f32_e32 v29, 0x3fd9db23, v28
	v_add_f32_e32 v25, 1.0, v25
	v_mul_f32_e32 v29, 0xbfb8aa3b, v29
	v_fmamk_f32 v27, v177, 0x3c800000, v13
	v_rcp_f32_e32 v25, v25
	v_exp_f32_e32 v29, v29
	v_med3_f32 v27, v27, s68, v221
	v_add_f32_e32 v27, 1.0, v27
	v_mul_f32_e32 v24, v24, v27
	v_mul_f32_e32 v27, v24, v25
	v_add_f32_e32 v25, 1.0, v29
	v_fmamk_f32 v24, v166, 0x3c800000, v6
	v_rcp_f32_e32 v25, v25
	v_med3_f32 v24, v24, s68, v221
	v_add_f32_e32 v24, 1.0, v24
	v_mul_f32_e32 v24, v28, v24
	v_mul_f32_e32 v28, v24, v25
	v_fmamk_f32 v24, v171, 0x3c800000, v3
	v_min_f32_e32 v24, 0x40e00000, v24
	v_mul_f32_e32 v25, 0x3fd9db23, v24
	v_mul_f32_e32 v25, 0xbfb8aa3b, v25
	v_exp_f32_e32 v25, v25
	v_fmamk_f32 v30, v172, 0x3c800000, v4
	v_min_f32_e32 v30, 0x40e00000, v30
	v_mul_f32_e32 v31, 0x3fd9db23, v30
	v_add_f32_e32 v25, 1.0, v25
	v_mul_f32_e32 v31, 0xbfb8aa3b, v31
	v_fmamk_f32 v29, v167, 0x3c800000, v7
	v_rcp_f32_e32 v25, v25
	v_exp_f32_e32 v31, v31
	v_med3_f32 v29, v29, s68, v221
	v_add_f32_e32 v29, 1.0, v29
	v_mul_f32_e32 v24, v24, v29
	v_mul_f32_e32 v29, v24, v25
	v_add_f32_e32 v25, 1.0, v31
	v_fmamk_f32 v24, v168, 0x3c800000, v8
	v_rcp_f32_e32 v25, v25
	v_med3_f32 v24, v24, s68, v221
	v_add_f32_e32 v24, 1.0, v24
	v_mul_f32_e32 v24, v30, v24
	v_mul_f32_e32 v30, v24, v25
	v_fmamk_f32 v24, v173, 0x3c800000, v5
	v_min_f32_e32 v24, 0x40e00000, v24
	v_mul_f32_e32 v31, 0x3fd9db23, v24
	v_mul_f32_e32 v31, 0xbfb8aa3b, v31
	v_exp_f32_e32 v31, v31
	v_fmamk_f32 v25, v169, 0x3c800000, v9
	v_med3_f32 v25, v25, s68, v221
	v_add_f32_e32 v25, 1.0, v25
	v_mul_f32_e32 v32, v24, v25
	v_add_f32_e32 v24, 1.0, v31
	v_rcp_f32_e32 v31, v24
	v_mov_b32_e32 v25, 0
	v_cvt_pk_fp8_f32 v25, v28, v29
	v_mov_b32_e32 v24, 0
	v_cvt_pk_fp8_f32 v24, v21, v23
	v_mul_f32_e32 v21, v32, v31
	v_cvt_pk_fp8_f32 v25, v30, v21 op_sel:[0,0,1]
	v_fmamk_f32 v21, v162, 0x3c800000, v14
	v_min_f32_e32 v21, 0x40e00000, v21
	v_cvt_pk_fp8_f32 v24, v26, v27 op_sel:[0,0,1]
	v_mul_f32_e32 v26, 0x3fd9db23, v21
	v_add_u32_e32 v22, 16, v20
	v_mul_f32_e32 v26, 0xbfb8aa3b, v26
	v_ashrrev_i32_e32 v23, 31, v22
	v_exp_f32_e32 v26, v26
	v_lshlrev_b64 v[22:23], 11, v[22:23]
	v_lshl_add_u64 v[22:23], s[6:7], 0, v[22:23]
	v_lshl_add_u64 v[22:23], v[22:23], 0, v[18:19]
	global_store_dwordx2 v[22:23], v[24:25], off
	v_fmamk_f32 v23, v158, 0x3c800000, v10
	v_add_f32_e32 v24, 1.0, v26
	v_rcp_f32_e32 v24, v24
	v_med3_f32 v23, v23, s68, v221
	v_add_f32_e32 v23, 1.0, v23
	v_mul_f32_e32 v21, v21, v23
	v_fmamk_f32 v23, v163, 0x3c800000, v15
	v_min_f32_e32 v23, 0x40e00000, v23
	v_mul_f32_e32 v21, v21, v24
	v_mul_f32_e32 v24, 0x3fd9db23, v23
	v_mul_f32_e32 v24, 0xbfb8aa3b, v24
	v_exp_f32_e32 v24, v24
	v_fmamk_f32 v26, v164, 0x3c800000, v16
	v_min_f32_e32 v26, 0x40e00000, v26
	v_mul_f32_e32 v27, 0x3fd9db23, v26
	v_mul_f32_e32 v27, 0xbfb8aa3b, v27
	v_add_f32_e32 v24, 1.0, v24
	v_exp_f32_e32 v27, v27
	v_fmamk_f32 v25, v159, 0x3c800000, v11
	v_rcp_f32_e32 v24, v24
	v_med3_f32 v25, v25, s68, v221
	v_add_f32_e32 v25, 1.0, v25
	v_mul_f32_e32 v23, v23, v25
	v_add_f32_e32 v25, 1.0, v27
	v_mul_f32_e32 v23, v23, v24
	v_fmamk_f32 v24, v160, 0x3c800000, v12
	v_rcp_f32_e32 v25, v25
	v_med3_f32 v24, v24, s68, v221
	v_add_f32_e32 v24, 1.0, v24
	v_mul_f32_e32 v24, v26, v24
	v_mul_f32_e32 v26, v24, v25
	v_fmamk_f32 v24, v165, 0x3c800000, v17
	v_min_f32_e32 v24, 0x40e00000, v24
	v_mul_f32_e32 v25, 0x3fd9db23, v24
	v_mul_f32_e32 v25, 0xbfb8aa3b, v25
	v_exp_f32_e32 v25, v25
	v_fmamk_f32 v28, v154, 0x3c800000, v2
	v_min_f32_e32 v28, 0x40e00000, v28
	v_mul_f32_e32 v29, 0x3fd9db23, v28
	v_add_f32_e32 v25, 1.0, v25
	v_mul_f32_e32 v29, 0xbfb8aa3b, v29
	v_fmamk_f32 v27, v161, 0x3c800000, v13
	v_rcp_f32_e32 v25, v25
	v_exp_f32_e32 v29, v29
	v_med3_f32 v27, v27, s68, v221
	v_add_f32_e32 v27, 1.0, v27
	v_mul_f32_e32 v24, v24, v27
	v_mul_f32_e32 v27, v24, v25
	v_add_f32_e32 v25, 1.0, v29
	v_fmamk_f32 v24, v150, 0x3c800000, v6
	v_rcp_f32_e32 v25, v25
	v_med3_f32 v24, v24, s68, v221
	v_add_f32_e32 v24, 1.0, v24
	v_mul_f32_e32 v24, v28, v24
	v_mul_f32_e32 v28, v24, v25
	v_fmamk_f32 v24, v155, 0x3c800000, v3
	v_min_f32_e32 v24, 0x40e00000, v24
	v_mul_f32_e32 v25, 0x3fd9db23, v24
	v_mul_f32_e32 v25, 0xbfb8aa3b, v25
	v_exp_f32_e32 v25, v25
	v_fmamk_f32 v30, v156, 0x3c800000, v4
	v_min_f32_e32 v30, 0x40e00000, v30
	v_mul_f32_e32 v31, 0x3fd9db23, v30
	v_add_f32_e32 v25, 1.0, v25
	v_mul_f32_e32 v31, 0xbfb8aa3b, v31
	v_fmamk_f32 v29, v151, 0x3c800000, v7
	v_rcp_f32_e32 v25, v25
	v_exp_f32_e32 v31, v31
	v_med3_f32 v29, v29, s68, v221
	v_add_f32_e32 v29, 1.0, v29
	v_mul_f32_e32 v24, v24, v29
; __device__ __forceinline__ float sigmoidf_(float x) { return __builtin_amdgcn_rcpf(1.f + __builtin_amdgcn_exp2f(-1.4426950408889634f * x)); }
; __device__ __forceinline__ unsigned pack_fp8x4(float a, float b, float c, float d) { int w = __builtin_amdgcn_cvt_pk_fp8_f32(a, b, 0, false); w = __builtin_amdgcn_cvt_pk_fp8_f32(c, d, w, true); return (unsigned)w; }
; #define ACT(t) (KBASE(t) <= qlo + QBLK - 1 && KBASE(t) + KVBLK - 1 >= qlo - W + 1)
;     __device__ __forceinline__ void operator()(const f32x4 (&acc)[2][2][4][2], const Unit& u, int wr, int wc, int fr, int fq) const {
;     ...
;             for (int m = 0; m < 4; ++m) { const size_t row = (size_t)(row0 + ai * HALF + m * 16);
;                 float a[8];
; #pragma unroll
;                 for (int n = 0; n < 2; ++n)
; #pragma unroll
;                     for (int i = 0; i < 4; ++i) { float g = acc[ai][0][m][n][i] * 0.015625f + bg[n][i], up = acc[ai][1][m][n][i] * 0.015625f + bu[n][i];
;                         g = fminf(g, 7.0f); up = fminf(fmaxf(up, -7.0f), 7.0f);
;                         a[4 * n + i] = (up + 1.0f) * g * sigmoidf_(1.702f * g); }
;                 uint2 w; w.x = pack_fp8x4(a[0], a[1], a[2], a[3]); w.y = pack_fp8x4(a[4], a[5], a[6], a[7]);
;                 *(uint2*)(ACT + row * 2048 + colL) = w; }
; template <class Epi, class Sched, bool ALIGN_EPI = false, bool SP2 = false, bool FP8 = false>
; __device__ __forceinline__ void gemm_phase(PG8_LAS unsigned char* lds, const Gemm g, const Sched& S, const Epi& E) {
;     ...
;         for (int t = 0; t < nt; t += 2) {
	v_mul_f32_e32 v29, v24, v25
	v_add_f32_e32 v25, 1.0, v31
	v_fmamk_f32 v24, v152, 0x3c800000, v8
	v_rcp_f32_e32 v25, v25
	v_med3_f32 v24, v24, s68, v221
	v_add_f32_e32 v24, 1.0, v24
	v_mul_f32_e32 v24, v30, v24
	v_mul_f32_e32 v30, v24, v25
	v_fmamk_f32 v24, v157, 0x3c800000, v5
	v_min_f32_e32 v24, 0x40e00000, v24
	v_mul_f32_e32 v31, 0x3fd9db23, v24
	v_mul_f32_e32 v31, 0xbfb8aa3b, v31
	v_exp_f32_e32 v31, v31
	v_fmamk_f32 v25, v153, 0x3c800000, v9
	v_med3_f32 v25, v25, s68, v221
	v_add_f32_e32 v25, 1.0, v25
	v_mul_f32_e32 v32, v24, v25
	v_add_f32_e32 v24, 1.0, v31
	v_rcp_f32_e32 v31, v24
	v_mov_b32_e32 v25, 0
	v_cvt_pk_fp8_f32 v25, v28, v29
	v_mov_b32_e32 v24, 0
	v_cvt_pk_fp8_f32 v24, v21, v23
	v_mul_f32_e32 v21, v32, v31
	v_cvt_pk_fp8_f32 v25, v30, v21 op_sel:[0,0,1]
	v_fmamk_f32 v21, v146, 0x3c800000, v14
	v_min_f32_e32 v21, 0x40e00000, v21
	v_cvt_pk_fp8_f32 v24, v26, v27 op_sel:[0,0,1]
	v_mul_f32_e32 v26, 0x3fd9db23, v21
	v_add_u32_e32 v22, 32, v20
	v_mul_f32_e32 v26, 0xbfb8aa3b, v26
	v_ashrrev_i32_e32 v23, 31, v22
	v_exp_f32_e32 v26, v26
	v_lshlrev_b64 v[22:23], 11, v[22:23]
	v_lshl_add_u64 v[22:23], s[6:7], 0, v[22:23]
	v_lshl_add_u64 v[22:23], v[22:23], 0, v[18:19]
	global_store_dwordx2 v[22:23], v[24:25], off
	v_fmamk_f32 v23, v142, 0x3c800000, v10
	v_add_f32_e32 v24, 1.0, v26
	v_rcp_f32_e32 v24, v24
	v_med3_f32 v23, v23, s68, v221
	v_add_f32_e32 v23, 1.0, v23
	v_mul_f32_e32 v21, v21, v23
	v_fmamk_f32 v23, v147, 0x3c800000, v15
	v_min_f32_e32 v23, 0x40e00000, v23
	v_mul_f32_e32 v21, v21, v24
	v_mul_f32_e32 v24, 0x3fd9db23, v23
	v_mul_f32_e32 v24, 0xbfb8aa3b, v24
	v_exp_f32_e32 v24, v24
	v_fmamk_f32 v26, v148, 0x3c800000, v16
	v_min_f32_e32 v26, 0x40e00000, v26
	v_mul_f32_e32 v27, 0x3fd9db23, v26
	v_mul_f32_e32 v27, 0xbfb8aa3b, v27
	v_add_f32_e32 v24, 1.0, v24
	v_exp_f32_e32 v27, v27
	v_fmamk_f32 v25, v143, 0x3c800000, v11
	v_rcp_f32_e32 v24, v24
	v_med3_f32 v25, v25, s68, v221
	v_add_f32_e32 v25, 1.0, v25
	v_mul_f32_e32 v23, v23, v25
	v_add_f32_e32 v25, 1.0, v27
	v_mul_f32_e32 v23, v23, v24
	v_fmamk_f32 v24, v144, 0x3c800000, v12
	v_rcp_f32_e32 v25, v25
	v_med3_f32 v24, v24, s68, v221
	v_add_f32_e32 v24, 1.0, v24
	v_mul_f32_e32 v24, v26, v24
	v_mul_f32_e32 v26, v24, v25
	v_fmamk_f32 v24, v149, 0x3c800000, v17
	v_min_f32_e32 v24, 0x40e00000, v24
	v_mul_f32_e32 v25, 0x3fd9db23, v24
	v_mul_f32_e32 v25, 0xbfb8aa3b, v25
	v_exp_f32_e32 v25, v25
	v_fmamk_f32 v28, v138, 0x3c800000, v2
	v_min_f32_e32 v28, 0x40e00000, v28
	v_mul_f32_e32 v29, 0x3fd9db23, v28
	v_add_f32_e32 v25, 1.0, v25
	v_mul_f32_e32 v29, 0xbfb8aa3b, v29
	v_fmamk_f32 v27, v145, 0x3c800000, v13
	v_rcp_f32_e32 v25, v25
	v_exp_f32_e32 v29, v29
	v_med3_f32 v27, v27, s68, v221
	v_add_f32_e32 v27, 1.0, v27
	v_mul_f32_e32 v24, v24, v27
	v_mul_f32_e32 v27, v24, v25
	v_add_f32_e32 v25, 1.0, v29
	v_fmamk_f32 v24, v134, 0x3c800000, v6
	v_rcp_f32_e32 v25, v25
	v_med3_f32 v24, v24, s68, v221
	v_add_f32_e32 v24, 1.0, v24
	v_mul_f32_e32 v24, v28, v24
	v_mul_f32_e32 v28, v24, v25
	v_fmamk_f32 v24, v139, 0x3c800000, v3
	v_min_f32_e32 v24, 0x40e00000, v24
	v_mul_f32_e32 v25, 0x3fd9db23, v24
	v_mul_f32_e32 v25, 0xbfb8aa3b, v25
	v_exp_f32_e32 v25, v25
	v_fmamk_f32 v30, v140, 0x3c800000, v4
	v_min_f32_e32 v30, 0x40e00000, v30
	v_mul_f32_e32 v31, 0x3fd9db23, v30
	v_add_f32_e32 v25, 1.0, v25
	v_mul_f32_e32 v31, 0xbfb8aa3b, v31
	v_fmamk_f32 v29, v135, 0x3c800000, v7
	v_rcp_f32_e32 v25, v25
	v_exp_f32_e32 v31, v31
	v_med3_f32 v29, v29, s68, v221
	v_add_f32_e32 v29, 1.0, v29
	v_mul_f32_e32 v24, v24, v29
	v_mul_f32_e32 v29, v24, v25
	v_add_f32_e32 v25, 1.0, v31
	v_fmamk_f32 v24, v136, 0x3c800000, v8
	v_rcp_f32_e32 v25, v25
	v_med3_f32 v24, v24, s68, v221
	v_add_f32_e32 v24, 1.0, v24
	v_mul_f32_e32 v24, v30, v24
	v_mul_f32_e32 v30, v24, v25
	v_fmamk_f32 v24, v141, 0x3c800000, v5
	v_min_f32_e32 v24, 0x40e00000, v24
	v_mul_f32_e32 v31, 0x3fd9db23, v24
	v_mul_f32_e32 v31, 0xbfb8aa3b, v31
	v_exp_f32_e32 v31, v31
	v_fmamk_f32 v25, v137, 0x3c800000, v9
	v_med3_f32 v25, v25, s68, v221
	v_add_f32_e32 v25, 1.0, v25
	v_mul_f32_e32 v32, v24, v25
	v_add_f32_e32 v24, 1.0, v31
	v_rcp_f32_e32 v31, v24
	v_mov_b32_e32 v24, 0
	v_mov_b32_e32 v25, 0
	v_cvt_pk_fp8_f32 v24, v21, v23
	v_cvt_pk_fp8_f32 v25, v28, v29
	v_add_u32_e32 v22, 48, v20
	v_mul_f32_e32 v21, v32, v31
	v_ashrrev_i32_e32 v23, 31, v22
	v_cvt_pk_fp8_f32 v24, v26, v27 op_sel:[0,0,1]
	v_cvt_pk_fp8_f32 v25, v30, v21 op_sel:[0,0,1]
	v_lshlrev_b64 v[22:23], 11, v[22:23]
	v_lshl_add_u64 v[22:23], s[6:7], 0, v[22:23]
	v_lshl_add_u64 v[22:23], v[22:23], 0, v[18:19]
	global_store_dwordx2 v[22:23], v[24:25], off
	s_cbranch_vccz .LBB0_1355
	s_andn2_b64 vcc, exec, s[26:27]
	s_mov_b64 s[2:3], -1
	s_cbranch_vccnz .LBB0_1334
	s_branch .LBB0_1356

; __global__ void __launch_bounds__(NWAVES * 64, 2) mk_fwd(Args args) {
	.amdhsa_kernel _Z6mk_fwd4Args
		.amdhsa_group_segment_fixed_size 0
		.amdhsa_private_segment_fixed_size 0
		.amdhsa_kernarg_size 480
		.amdhsa_user_sgpr_count 2
		.amdhsa_user_sgpr_dispatch_ptr 0
		.amdhsa_user_sgpr_queue_ptr 0
		.amdhsa_user_sgpr_kernarg_segment_ptr 1
		.amdhsa_user_sgpr_dispatch_id 0
		.amdhsa_user_sgpr_kernarg_preload_length 0
		.amdhsa_user_sgpr_kernarg_preload_offset 0
		.amdhsa_user_sgpr_private_segment_size 0
		.amdhsa_uses_dynamic_stack 0
		.amdhsa_enable_private_segment 0
		.amdhsa_system_sgpr_workgroup_id_x 1
		.amdhsa_system_sgpr_workgroup_id_y 0
		.amdhsa_system_sgpr_workgroup_id_z 0
		.amdhsa_system_sgpr_workgroup_info 0
		.amdhsa_system_vgpr_workitem_id 0
		.amdhsa_next_free_vgpr 256
		.amdhsa_next_free_sgpr 100
		.amdhsa_accum_offset 256
		.amdhsa_reserve_vcc 1
		.amdhsa_float_round_mode_32 0
		.amdhsa_float_round_mode_16_64 0
		.amdhsa_float_denorm_mode_32 3
		.amdhsa_float_denorm_mode_16_64 3
		.amdhsa_dx10_clamp 1
		.amdhsa_ieee_mode 1
		.amdhsa_fp16_overflow 0
		.amdhsa_tg_split 0
		.amdhsa_exception_fp_ieee_invalid_op 0
		.amdhsa_exception_fp_denorm_src 0
		.amdhsa_exception_fp_ieee_div_zero 0
		.amdhsa_exception_fp_ieee_overflow 0
		.amdhsa_exception_fp_ieee_underflow 0
		.amdhsa_exception_fp_ieee_inexact 0
		.amdhsa_exception_int_div_zero 0
	.end_amdhsa_kernel

; __global__ void __launch_bounds__(NWAVES * 64, 2) mk_fwd(Args args) {
amdhsa.kernels:
  - .agpr_count:     0
    .args:
      - .offset:         0
        .size:           224
        .value_kind:     by_value
      - .offset:         224
        .size:           4
        .value_kind:     hidden_block_count_x
      - .offset:         228
        .size:           4
        .value_kind:     hidden_block_count_y
      - .offset:         232
        .size:           4
        .value_kind:     hidden_block_count_z
      - .offset:         236
        .size:           2
        .value_kind:     hidden_group_size_x
      - .offset:         238
        .size:           2
        .value_kind:     hidden_group_size_y
      - .offset:         240
        .size:           2
        .value_kind:     hidden_group_size_z
      - .offset:         242
        .size:           2
        .value_kind:     hidden_remainder_x
      - .offset:         244
        .size:           2
        .value_kind:     hidden_remainder_y
      - .offset:         246
        .size:           2
        .value_kind:     hidden_remainder_z
      - .offset:         264
        .size:           8
        .value_kind:     hidden_global_offset_x
      - .offset:         272
        .size:           8
        .value_kind:     hidden_global_offset_y
      - .offset:         280
        .size:           8
        .value_kind:     hidden_global_offset_z
      - .offset:         288
        .size:           2
        .value_kind:     hidden_grid_dims
      - .offset:         344
        .size:           4
        .value_kind:     hidden_dynamic_lds_size
    .group_segment_fixed_size: 0
    .kernarg_segment_align: 8
    .kernarg_segment_size: 480
    .language:       OpenCL C
    .language_version:
      - 2
      - 0
    .max_flat_workgroup_size: 512
    .name:           _Z6mk_fwd4Args
    .private_segment_fixed_size: 0
    .sgpr_count:     106
    .sgpr_spill_count: 109
    .symbol:         _Z6mk_fwd4Args.kd
    .uniform_work_group_size: 1
    .uses_dynamic_stack: false
    .vgpr_count:     256
    .vgpr_spill_count: 0
    .wavefront_size: 64
